# adds low-rank prep unit: weight fragments of a whole column group prefetched before the previous epilogue (6 slots)
# speedup vs baseline: 1.0057x; 1.0057x over previous
.LBB0_284:
	s_or_b64 exec, exec, s[36:37]
	s_waitcnt vmcnt(0)
	v_sub_f32_e32 v24, v39, v35
	v_fmac_f32_e32 v35, v38, v24
	v_add_f32_e32 v24, v35, v35
	v_sub_f32_e32 v2, v2, v20
	v_cndmask_b32_e64 v31, 0, v31, s[4:5]
	v_mul_f32_e32 v24, 0x3fb8aa3b, v24
	v_fmac_f32_e32 v20, v37, v2
	v_sub_f32_e32 v2, v31, v23
	v_exp_f32_e32 v24, v24
	v_fmac_f32_e32 v23, v2, v36
	v_add_f32_e32 v2, v23, v23
	v_mul_f32_e32 v2, 0x3fb8aa3b, v2
	v_exp_f32_e32 v2, v2
	v_add_f32_e32 v24, 1.0, v24
	v_rcp_f32_e32 v24, v24
	v_cvt_pk_bf16_f32 v31, v20, s0
	v_add_f32_e32 v2, 1.0, v2
	v_rcp_f32_e32 v2, v2
	v_fma_f32 v24, v24, -2.0, 1.0
	v_cvt_pk_bf16_f32 v35, v24, s0
	ds_write_b16 v135, v35
	v_lshlrev_b32_e32 v35, 16, v35
	v_lshlrev_b32_e32 v23, 16, v31
	v_cndmask_b32_e64 v19, 0, v19, s[4:5]
	v_sub_f32_e32 v24, v24, v35
	v_sub_f32_e32 v20, v20, v23
	v_fma_f32 v2, v2, -2.0, 1.0
	v_sub_f32_e32 v19, v19, v5
	v_cvt_pk_bf16_f32 v24, v24, s0
	v_cvt_pk_bf16_f32 v20, v20, s0
	v_fmac_f32_e32 v5, v19, v34
	v_cvt_pk_bf16_f32 v19, v2, s0
	ds_write_b16 v135, v24 offset:6656
	ds_write_b16 v135, v31 offset:13312
	ds_write_b16 v135, v20 offset:19968
	ds_write_b16 v136, v19 offset:1024
	v_lshlrev_b32_e32 v19, 16, v19
	v_sub_f32_e32 v2, v2, v19
	v_cvt_pk_bf16_f32 v2, v2, s0
	ds_write_b16 v136, v2 offset:7680
	v_cndmask_b32_e32 v2, 0, v13, vcc
	v_sub_f32_e32 v2, v2, v8
	v_fmac_f32_e32 v8, v2, v30
	v_add_f32_e32 v2, v8, v8
	v_mul_f32_e32 v2, 0x3fb8aa3b, v2
	v_exp_f32_e32 v2, v2
	v_cvt_pk_bf16_f32 v20, v5, s0
	v_lshlrev_b32_e32 v8, 16, v20
	v_sub_f32_e32 v5, v5, v8
	v_add_f32_e32 v2, 1.0, v2
	v_rcp_f32_e32 v2, v2
	v_cvt_pk_bf16_f32 v5, v5, s0
	ds_write_b16 v136, v5 offset:20992
	v_cndmask_b32_e32 v5, 0, v33, vcc
	v_fma_f32 v2, v2, -2.0, 1.0
	v_sub_f32_e32 v5, v5, v22
	v_fmac_f32_e32 v22, v5, v25
	v_cvt_pk_bf16_f32 v5, v2, s0
	ds_write_b16 v136, v20 offset:14336
	ds_write_b16 v137, v5 offset:2048
	v_lshlrev_b32_e32 v5, 16, v5
	v_sub_f32_e32 v2, v2, v5
	v_cvt_pk_bf16_f32 v2, v2, s0
	ds_write_b16 v137, v2 offset:8704
	v_cndmask_b32_e64 v2, 0, v29, s[0:1]
	v_sub_f32_e32 v2, v2, v26
	v_fmac_f32_e32 v26, v2, v16
	v_add_f32_e32 v2, v26, v26
	v_mul_f32_e32 v2, 0x3fb8aa3b, v2
	v_exp_f32_e32 v2, v2
	v_cvt_pk_bf16_f32 v8, v22, s0
	v_lshlrev_b32_e32 v5, 16, v8
	v_sub_f32_e32 v5, v22, v5
	v_add_f32_e32 v2, 1.0, v2
	v_rcp_f32_e32 v2, v2
	v_cvt_pk_bf16_f32 v5, v5, s0
	ds_write_b16 v137, v5 offset:22016
	v_cndmask_b32_e64 v5, 0, v21, s[0:1]
	v_fma_f32 v2, v2, -2.0, 1.0
	v_sub_f32_e32 v5, v5, v6
	v_fmac_f32_e32 v6, v5, v7
	v_cvt_pk_bf16_f32 v5, v2, s0
	ds_write_b16 v137, v8 offset:15360
	ds_write_b16 v138, v5 offset:3072
	v_lshlrev_b32_e32 v5, 16, v5
	v_sub_f32_e32 v2, v2, v5
	v_cvt_pk_bf16_f32 v2, v2, s0
	ds_write_b16 v138, v2 offset:9728
	v_cndmask_b32_e64 v2, 0, v14, s[8:9]
	v_sub_f32_e32 v2, v2, v9
	v_fmac_f32_e32 v9, v2, v32
	v_add_f32_e32 v2, v9, v9
	v_mul_f32_e32 v2, 0x3fb8aa3b, v2
	v_exp_f32_e32 v2, v2
	v_cvt_pk_bf16_f32 v7, v6, s0
	v_lshlrev_b32_e32 v5, 16, v7
	v_sub_f32_e32 v5, v6, v5
	v_add_f32_e32 v2, 1.0, v2
	v_rcp_f32_e32 v2, v2
	v_cvt_pk_bf16_f32 v5, v5, s0
	ds_write_b16 v138, v5 offset:23040
	v_cndmask_b32_e64 v5, 0, v27, s[8:9]
	v_fma_f32 v2, v2, -2.0, 1.0
	v_sub_f32_e32 v5, v5, v12
	v_fmac_f32_e32 v12, v5, v28
	v_cvt_pk_bf16_f32 v5, v2, s0
	ds_write_b16 v138, v7 offset:16384
	ds_write_b16 v139, v5 offset:4096
	v_lshlrev_b32_e32 v5, 16, v5
	v_sub_f32_e32 v2, v2, v5
	v_cvt_pk_bf16_f32 v2, v2, s0
	ds_write_b16 v139, v2 offset:10752
	v_cndmask_b32_e64 v2, 0, v17, s[6:7]
	v_sub_f32_e32 v2, v2, v15
	v_fmac_f32_e32 v15, v2, v18
	v_add_f32_e32 v2, v15, v15
	v_mul_f32_e32 v2, 0x3fb8aa3b, v2
	v_exp_f32_e32 v2, v2
	v_cvt_pk_bf16_f32 v6, v12, s0
	v_lshlrev_b32_e32 v5, 16, v6
	v_sub_f32_e32 v5, v12, v5
	v_add_f32_e32 v2, 1.0, v2
	v_rcp_f32_e32 v2, v2
	v_cvt_pk_bf16_f32 v5, v5, s0
	ds_write_b16 v139, v5 offset:24064
	v_cndmask_b32_e64 v5, 0, v10, s[6:7]
	v_fma_f32 v2, v2, -2.0, 1.0
	v_sub_f32_e32 v5, v5, v4
	v_fmac_f32_e32 v4, v5, v11
	v_cvt_pk_bf16_f32 v5, v2, s0
	ds_write_b16 v139, v6 offset:17408
	ds_write_b16 v140, v5 offset:5120
	v_lshlrev_b32_e32 v5, 16, v5
	v_sub_f32_e32 v2, v2, v5
	v_cvt_pk_bf16_f32 v6, v4, s0
	v_cvt_pk_bf16_f32 v2, v2, s0
	ds_write_b16 v140, v2 offset:11776
	ds_write_b16 v140, v6 offset:18432
	v_lshlrev_b32_e32 v2, 16, v6
	v_sub_f32_e32 v2, v4, v2
	v_cvt_pk_bf16_f32 v2, v2, s0
	ds_write_b16 v140, v2 offset:25088
	s_waitcnt lgkmcnt(0)
	s_barrier
	global_load_dwordx4 v[36:39], v[98:99], off
	global_load_dwordx4 v[52:55], v[100:101], off
	global_load_dwordx4 v[48:51], v[102:103], off
	global_load_dwordx4 v[64:67], v[104:105], off
	global_load_dwordx4 v[44:47], v[98:99], off offset:32
	global_load_dwordx4 v[56:59], v[100:101], off offset:32
	global_load_dwordx4 v[40:43], v[102:103], off offset:32
	global_load_dwordx4 v[60:63], v[104:105], off offset:32
	global_load_dwordx4 v[154:157], v[98:99], off offset:64
	global_load_dwordx4 v[158:161], v[100:101], off offset:64
	global_load_dwordx4 v[178:181], v[102:103], off offset:64
	global_load_dwordx4 v[182:185], v[104:105], off offset:64
	global_load_dwordx4 v[186:189], v[98:99], off offset:96
	global_load_dwordx4 v[190:193], v[100:101], off offset:96
	global_load_dwordx4 v[194:197], v[102:103], off offset:96
	global_load_dwordx4 v[198:201], v[104:105], off offset:96
	global_load_dwordx4 v[202:205], v[98:99], off offset:128
	global_load_dwordx4 v[218:221], v[100:101], off offset:128
	global_load_dwordx4 v[222:225], v[102:103], off offset:128
	global_load_dwordx4 v[226:229], v[104:105], off offset:128
	global_load_dword v148, v[114:115], off
	global_load_dword v147, v[116:117], off
	s_mov_b32 s0, 32
	v_mov_b32_e32 v2, v146
	s_waitcnt vmcnt(0)
.LBB0_285:
	v_add_u32_e32 v162, 0x18000, v2
	v_mov_b32_e32 v163, v3
	v_lshl_add_u64 v[172:173], v[162:163], 1, v[96:97]
	v_add_u32_e32 v162, 0x30000, v2
	v_lshl_add_u64 v[170:171], v[2:3], 1, v[96:97]
	v_lshl_add_u64 v[174:175], v[162:163], 1, v[96:97]
	v_add_u32_e32 v162, 0x48000, v2
	v_lshl_add_u64 v[176:177], v[162:163], 1, v[96:97]
	global_load_dwordx4 v[68:71], v[170:171], off offset:160
	global_load_dwordx4 v[150:153], v[172:173], off offset:160
	global_load_dwordx4 v[230:233], v[174:175], off offset:160
	global_load_dwordx4 v[248:251], v[176:177], off offset:160
	ds_read_b128 v[162:165], v142
	ds_read_b128 v[166:169], v142 offset:13312
	ds_read_b128 v[240:243], v143
	ds_read_b128 v[244:247], v144
	s_waitcnt vmcnt(54) lgkmcnt(2)
	v_mfma_f32_32x32x16_bf16 v[20:35], v[162:165], v[36:39], 0
	v_mfma_f32_32x32x16_bf16 v[4:19], v[166:169], v[48:51], 0
	v_mfma_f32_32x32x16_bf16 v[20:35], v[162:165], v[52:55], v[20:35]
	v_mfma_f32_32x32x16_bf16 v[4:19], v[166:169], v[64:67], v[4:19]
	ds_read_b128 v[162:165], v142 offset:32
	ds_read_b128 v[166:169], v142 offset:13344
	s_waitcnt lgkmcnt(2)
	v_mfma_f32_32x32x16_bf16 v[20:35], v[240:243], v[36:39], v[20:35]
	v_mfma_f32_32x32x16_bf16 v[4:19], v[244:247], v[48:51], v[4:19]
	ds_read_b128 v[240:243], v143 offset:32
	ds_read_b128 v[244:247], v144 offset:32
	s_waitcnt vmcnt(50) lgkmcnt(2)
	v_mfma_f32_32x32x16_bf16 v[20:35], v[162:165], v[44:47], v[20:35]
	v_mfma_f32_32x32x16_bf16 v[4:19], v[166:169], v[40:43], v[4:19]
	v_mfma_f32_32x32x16_bf16 v[20:35], v[162:165], v[56:59], v[20:35]
	v_mfma_f32_32x32x16_bf16 v[4:19], v[166:169], v[60:63], v[4:19]
	ds_read_b128 v[162:165], v142 offset:64
	ds_read_b128 v[166:169], v142 offset:13376
	s_waitcnt lgkmcnt(2)
	v_mfma_f32_32x32x16_bf16 v[20:35], v[240:243], v[44:47], v[20:35]
	v_mfma_f32_32x32x16_bf16 v[4:19], v[244:247], v[40:43], v[4:19]
	ds_read_b128 v[240:243], v143 offset:64
	ds_read_b128 v[244:247], v144 offset:64
	s_waitcnt vmcnt(46) lgkmcnt(2)
	v_mfma_f32_32x32x16_bf16 v[20:35], v[162:165], v[154:157], v[20:35]
	v_mfma_f32_32x32x16_bf16 v[4:19], v[166:169], v[178:181], v[4:19]
	v_mfma_f32_32x32x16_bf16 v[20:35], v[162:165], v[158:161], v[20:35]
	v_mfma_f32_32x32x16_bf16 v[4:19], v[166:169], v[182:185], v[4:19]
	ds_read_b128 v[162:165], v142 offset:96
	ds_read_b128 v[166:169], v142 offset:13408
	s_waitcnt lgkmcnt(2)
	v_mfma_f32_32x32x16_bf16 v[20:35], v[240:243], v[154:157], v[20:35]
	v_mfma_f32_32x32x16_bf16 v[4:19], v[244:247], v[178:181], v[4:19]
	ds_read_b128 v[240:243], v143 offset:96
	ds_read_b128 v[244:247], v144 offset:96
	s_waitcnt vmcnt(42) lgkmcnt(2)
	v_mfma_f32_32x32x16_bf16 v[20:35], v[162:165], v[186:189], v[20:35]
	v_mfma_f32_32x32x16_bf16 v[4:19], v[166:169], v[194:197], v[4:19]
	v_mfma_f32_32x32x16_bf16 v[20:35], v[162:165], v[190:193], v[20:35]
	v_mfma_f32_32x32x16_bf16 v[4:19], v[166:169], v[198:201], v[4:19]
	ds_read_b128 v[162:165], v142 offset:128
	ds_read_b128 v[166:169], v142 offset:13440
	s_waitcnt lgkmcnt(2)
	v_mfma_f32_32x32x16_bf16 v[20:35], v[240:243], v[186:189], v[20:35]
	v_mfma_f32_32x32x16_bf16 v[4:19], v[244:247], v[194:197], v[4:19]
	ds_read_b128 v[240:243], v143 offset:128
	ds_read_b128 v[244:247], v144 offset:128
	s_waitcnt vmcnt(38) lgkmcnt(2)
	v_mfma_f32_32x32x16_bf16 v[20:35], v[162:165], v[202:205], v[20:35]
	v_mfma_f32_32x32x16_bf16 v[4:19], v[166:169], v[222:225], v[4:19]
	v_mfma_f32_32x32x16_bf16 v[20:35], v[162:165], v[218:221], v[20:35]
	v_mfma_f32_32x32x16_bf16 v[4:19], v[166:169], v[226:229], v[4:19]
	ds_read_b128 v[162:165], v142 offset:160
	ds_read_b128 v[166:169], v142 offset:13472
	s_waitcnt lgkmcnt(2)
	v_mfma_f32_32x32x16_bf16 v[20:35], v[240:243], v[202:205], v[20:35]
	v_mfma_f32_32x32x16_bf16 v[4:19], v[244:247], v[222:225], v[4:19]
	ds_read_b128 v[240:243], v143 offset:160
	ds_read_b128 v[244:247], v144 offset:160
	s_waitcnt vmcnt(0) lgkmcnt(2)
	v_mfma_f32_32x32x16_bf16 v[20:35], v[162:165], v[68:71], v[20:35]
	v_mfma_f32_32x32x16_bf16 v[4:19], v[166:169], v[230:233], v[4:19]
	v_mfma_f32_32x32x16_bf16 v[20:35], v[162:165], v[150:153], v[20:35]
	v_mfma_f32_32x32x16_bf16 v[4:19], v[166:169], v[248:251], v[4:19]
	s_waitcnt lgkmcnt(0)
	v_mfma_f32_32x32x16_bf16 v[20:35], v[240:243], v[68:71], v[20:35]
	v_mfma_f32_32x32x16_bf16 v[4:19], v[244:247], v[230:233], v[4:19]
	s_cmpk_lg_i32 s0, 0x80
	s_cselect_b32 s1, s0, 0x60
	v_add_u32_e32 v149, s1, v141
	s_cbranch_scc0 .Llr_nopref
	v_mul_lo_u32 v162, v149, s53
	v_mov_b32_e32 v163, v3
	v_add_u32_e32 v164, 0x18000, v162
	v_mov_b32_e32 v165, v3
	v_lshl_add_u64 v[170:171], v[162:163], 1, v[96:97]
	v_lshl_add_u64 v[172:173], v[164:165], 1, v[96:97]
	v_add_u32_e32 v164, 0x30000, v162
	v_add_u32_e32 v162, 0x48000, v162
	v_lshl_add_u64 v[174:175], v[164:165], 1, v[96:97]
	v_lshl_add_u64 v[176:177], v[162:163], 1, v[96:97]
	global_load_dwordx4 v[36:39], v[170:171], off
	global_load_dwordx4 v[52:55], v[172:173], off
	global_load_dwordx4 v[48:51], v[174:175], off
	global_load_dwordx4 v[64:67], v[176:177], off
	global_load_dwordx4 v[44:47], v[170:171], off offset:32
	global_load_dwordx4 v[56:59], v[172:173], off offset:32
	global_load_dwordx4 v[40:43], v[174:175], off offset:32
	global_load_dwordx4 v[60:63], v[176:177], off offset:32
	global_load_dwordx4 v[154:157], v[170:171], off offset:64
	global_load_dwordx4 v[158:161], v[172:173], off offset:64
	global_load_dwordx4 v[178:181], v[174:175], off offset:64
	global_load_dwordx4 v[182:185], v[176:177], off offset:64
	global_load_dwordx4 v[186:189], v[170:171], off offset:96
	global_load_dwordx4 v[190:193], v[172:173], off offset:96
	global_load_dwordx4 v[194:197], v[174:175], off offset:96
	global_load_dwordx4 v[198:201], v[176:177], off offset:96
	global_load_dwordx4 v[202:205], v[170:171], off offset:128
	global_load_dwordx4 v[218:221], v[172:173], off offset:128
	global_load_dwordx4 v[222:225], v[174:175], off offset:128
	global_load_dwordx4 v[226:229], v[176:177], off offset:128
.Llr_nopref:
	v_add_u32_e32 v68, s12, v149
	v_ashrrev_i32_e32 v69, 31, v68
	v_lshlrev_b64 v[70:71], 2, v[68:69]
	v_lshl_add_u64 v[68:69], s[30:31], 0, v[70:71]
	v_lshl_add_u64 v[70:71], s[66:67], 0, v[70:71]
	global_load_dword v68, v[68:69], off
	s_nop 0
	global_load_dword v69, v[70:71], off
	v_add_f32_e32 v4, v147, v4
	v_mul_f32_e32 v4, 0xbfb8aa3b, v4
	v_exp_f32_e32 v4, v4
	v_add_u32_e32 v70, s0, v145
	v_subrev_u32_e32 v150, 32, v70
	v_add_f32_e32 v20, v148, v20
	v_add_f32_e32 v4, 1.0, v4
	v_rcp_f32_e32 v4, v4
	v_mov_b32_e32 v151, v3
	v_mul_f32_e32 v20, 0xbfb8aa3b, v20
	v_lshl_add_u64 v[152:153], v[150:151], 2, s[58:59]
	v_cvt_pk_bf16_f32 v4, v4, s0
	v_lshl_add_u64 v[150:151], v[150:151], 1, s[56:57]
	v_exp_f32_e32 v20, v20
	global_store_short v[150:151], v4, off
	v_add_f32_e32 v4, v148, v21
	v_mul_f32_e32 v4, 0xbfb8aa3b, v4
	v_exp_f32_e32 v4, v4
	v_add_f32_e32 v20, 1.0, v20
	v_rcp_f32_e32 v20, v20
	v_mov_b32_e32 v21, v3
	v_add_f32_e32 v4, 1.0, v4
	v_rcp_f32_e32 v4, v4
	v_mul_f32_e32 v20, 0xbf1b459e, v20
	v_mul_f32_e32 v20, 0x3fb8aa3b, v20
	v_exp_f32_e32 v20, v20
	v_mul_f32_e32 v4, 0xbf1b459e, v4
	v_mul_f32_e32 v4, 0x3fb8aa3b, v4
	v_exp_f32_e32 v4, v4
	global_store_dword v[152:153], v20, off
	v_add_u32_e32 v20, 0x3e0, v70
	v_lshl_add_u64 v[150:151], v[20:21], 2, s[58:59]
	global_store_dword v[150:151], v4, off
	v_add_f32_e32 v4, v147, v5
	v_mul_f32_e32 v4, 0xbfb8aa3b, v4
	v_exp_f32_e32 v4, v4
	v_add_f32_e32 v6, v147, v6
	v_mul_f32_e32 v6, 0xbfb8aa3b, v6
	v_exp_f32_e32 v6, v6
	v_add_f32_e32 v4, 1.0, v4
	v_rcp_f32_e32 v4, v4
	v_add_u32_e32 v2, 0xc00, v2
	v_add_f32_e32 v6, 1.0, v6
	v_rcp_f32_e32 v6, v6
	v_cvt_pk_bf16_f32 v71, v4, s0
	v_lshl_add_u64 v[4:5], v[20:21], 1, s[56:57]
	global_store_short v[4:5], v71, off
	v_add_f32_e32 v5, v148, v22
	v_mul_f32_e32 v5, 0xbfb8aa3b, v5
	v_exp_f32_e32 v5, v5
	v_add_u32_e32 v4, 0x7e0, v70
	v_cvt_pk_bf16_f32 v6, v6, s0
	v_add_f32_e32 v5, 1.0, v5
	v_rcp_f32_e32 v5, v5
	s_nop 0
	v_mul_f32_e32 v5, 0xbf1b459e, v5
	v_mul_f32_e32 v5, 0x3fb8aa3b, v5
	v_exp_f32_e32 v22, v5
	v_mov_b32_e32 v5, v3
	v_lshl_add_u64 v[20:21], v[4:5], 2, s[58:59]
	v_lshl_add_u64 v[4:5], v[4:5], 1, s[56:57]
	global_store_short v[4:5], v6, off
	v_add_f32_e32 v5, v148, v23
	v_mul_f32_e32 v5, 0xbfb8aa3b, v5
	v_exp_f32_e32 v5, v5
	v_add_u32_e32 v4, 0xbe0, v70
	global_store_dword v[20:21], v22, off
	v_add_f32_e32 v5, 1.0, v5
	v_rcp_f32_e32 v5, v5
	s_nop 0
	v_mul_f32_e32 v5, 0xbf1b459e, v5
	v_mul_f32_e32 v5, 0x3fb8aa3b, v5
	v_exp_f32_e32 v6, v5
	v_mov_b32_e32 v5, v3
	v_lshl_add_u64 v[20:21], v[4:5], 2, s[58:59]
	v_lshl_add_u64 v[4:5], v[4:5], 1, s[56:57]
	global_store_dword v[20:21], v6, off
	v_add_f32_e32 v6, v147, v7
	v_mul_f32_e32 v6, 0xbfb8aa3b, v6
	v_exp_f32_e32 v6, v6
	s_nop 0
	v_add_f32_e32 v6, 1.0, v6
	v_rcp_f32_e32 v6, v6
	s_nop 0
	v_cvt_pk_bf16_f32 v6, v6, s0
	global_store_short v[4:5], v6, off
	v_add_f32_e32 v5, v148, v24
	v_mul_f32_e32 v5, 0xbfb8aa3b, v5
	v_exp_f32_e32 v5, v5
	v_add_u32_e32 v4, 0x1fe0, v70
	v_add_f32_e32 v5, 1.0, v5
	v_rcp_f32_e32 v5, v5
	s_nop 0
	v_mul_f32_e32 v5, 0xbf1b459e, v5
	v_mul_f32_e32 v5, 0x3fb8aa3b, v5
	v_exp_f32_e32 v20, v5
	v_mov_b32_e32 v5, v3
	v_lshl_add_u64 v[6:7], v[4:5], 2, s[58:59]
	v_lshl_add_u64 v[4:5], v[4:5], 1, s[56:57]
	global_store_dword v[6:7], v20, off
	v_add_f32_e32 v6, v147, v8
	v_mul_f32_e32 v6, 0xbfb8aa3b, v6
	v_exp_f32_e32 v6, v6
	s_nop 0
	v_add_f32_e32 v6, 1.0, v6
	v_rcp_f32_e32 v6, v6
	s_nop 0
	v_cvt_pk_bf16_f32 v6, v6, s0
	global_store_short v[4:5], v6, off
	v_add_f32_e32 v5, v148, v25
	v_mul_f32_e32 v5, 0xbfb8aa3b, v5
	v_exp_f32_e32 v5, v5
	v_add_u32_e32 v4, 0x23e0, v70
	v_add_f32_e32 v5, 1.0, v5
	v_rcp_f32_e32 v5, v5
	s_nop 0
	v_mul_f32_e32 v5, 0xbf1b459e, v5
	v_mul_f32_e32 v5, 0x3fb8aa3b, v5
	v_exp_f32_e32 v8, v5
	v_mov_b32_e32 v5, v3
	v_lshl_add_u64 v[6:7], v[4:5], 2, s[58:59]
	v_lshl_add_u64 v[4:5], v[4:5], 1, s[56:57]
	global_store_dword v[6:7], v8, off
	v_add_f32_e32 v6, v147, v9
	v_mul_f32_e32 v6, 0xbfb8aa3b, v6
	v_exp_f32_e32 v6, v6
	s_nop 0
	v_add_f32_e32 v6, 1.0, v6
	v_rcp_f32_e32 v6, v6
	s_nop 0
	v_cvt_pk_bf16_f32 v6, v6, s0
	global_store_short v[4:5], v6, off
	v_add_f32_e32 v5, v148, v26
	v_mul_f32_e32 v5, 0xbfb8aa3b, v5
	v_exp_f32_e32 v5, v5
	v_add_u32_e32 v4, 0x27e0, v70
	v_add_f32_e32 v5, 1.0, v5
	v_rcp_f32_e32 v5, v5
	s_nop 0
	v_mul_f32_e32 v5, 0xbf1b459e, v5
	v_mul_f32_e32 v5, 0x3fb8aa3b, v5
	v_exp_f32_e32 v8, v5
	v_mov_b32_e32 v5, v3
	v_lshl_add_u64 v[6:7], v[4:5], 2, s[58:59]
	v_lshl_add_u64 v[4:5], v[4:5], 1, s[56:57]
	global_store_dword v[6:7], v8, off
	v_add_f32_e32 v6, v147, v10
	v_mul_f32_e32 v6, 0xbfb8aa3b, v6
	v_exp_f32_e32 v6, v6
	s_nop 0
	v_add_f32_e32 v6, 1.0, v6
	v_rcp_f32_e32 v6, v6
	s_nop 0
	v_cvt_pk_bf16_f32 v6, v6, s0
	global_store_short v[4:5], v6, off
	v_add_f32_e32 v5, v148, v27
	v_mul_f32_e32 v5, 0xbfb8aa3b, v5
	v_exp_f32_e32 v5, v5
	v_add_u32_e32 v4, 0x2be0, v70
	v_add_f32_e32 v5, 1.0, v5
	v_rcp_f32_e32 v5, v5
	s_nop 0
	v_mul_f32_e32 v5, 0xbf1b459e, v5
	v_mul_f32_e32 v5, 0x3fb8aa3b, v5
	v_exp_f32_e32 v8, v5
	v_mov_b32_e32 v5, v3
	v_lshl_add_u64 v[6:7], v[4:5], 2, s[58:59]
	v_lshl_add_u64 v[4:5], v[4:5], 1, s[56:57]
	global_store_dword v[6:7], v8, off
	v_add_f32_e32 v6, v147, v11
	v_mul_f32_e32 v6, 0xbfb8aa3b, v6
	v_exp_f32_e32 v6, v6
	s_nop 0
	v_add_f32_e32 v6, 1.0, v6
	v_rcp_f32_e32 v6, v6
	s_nop 0
	v_cvt_pk_bf16_f32 v6, v6, s0
	global_store_short v[4:5], v6, off
	v_add_f32_e32 v5, v148, v28
	v_mul_f32_e32 v5, 0xbfb8aa3b, v5
	v_exp_f32_e32 v5, v5
	v_add_u32_e32 v4, 0x3fe0, v70
	v_add_f32_e32 v5, 1.0, v5
	v_rcp_f32_e32 v5, v5
	s_nop 0
	v_mul_f32_e32 v5, 0xbf1b459e, v5
	v_mul_f32_e32 v5, 0x3fb8aa3b, v5
	v_exp_f32_e32 v8, v5
	v_mov_b32_e32 v5, v3
	v_lshl_add_u64 v[6:7], v[4:5], 2, s[58:59]
	v_lshl_add_u64 v[4:5], v[4:5], 1, s[56:57]
	global_store_dword v[6:7], v8, off
	v_add_f32_e32 v6, v147, v12
	v_mul_f32_e32 v6, 0xbfb8aa3b, v6
	v_exp_f32_e32 v6, v6
	s_nop 0
	v_add_f32_e32 v6, 1.0, v6
	v_rcp_f32_e32 v6, v6
	s_nop 0
	v_cvt_pk_bf16_f32 v6, v6, s0
	global_store_short v[4:5], v6, off
	v_add_f32_e32 v5, v148, v29
	v_mul_f32_e32 v5, 0xbfb8aa3b, v5
	v_exp_f32_e32 v5, v5
	v_add_u32_e32 v4, 0x43e0, v70
	v_add_f32_e32 v5, 1.0, v5
	v_rcp_f32_e32 v5, v5
	s_nop 0
	v_mul_f32_e32 v5, 0xbf1b459e, v5
	v_mul_f32_e32 v5, 0x3fb8aa3b, v5
	v_exp_f32_e32 v8, v5
	v_mov_b32_e32 v5, v3
	v_lshl_add_u64 v[6:7], v[4:5], 2, s[58:59]
	v_lshl_add_u64 v[4:5], v[4:5], 1, s[56:57]
	global_store_dword v[6:7], v8, off
	v_add_f32_e32 v6, v147, v13
	v_mul_f32_e32 v6, 0xbfb8aa3b, v6
	v_exp_f32_e32 v6, v6
	s_nop 0
	v_add_f32_e32 v6, 1.0, v6
	v_rcp_f32_e32 v6, v6
	s_nop 0
	v_cvt_pk_bf16_f32 v6, v6, s0
	global_store_short v[4:5], v6, off
	v_add_f32_e32 v5, v148, v30
	v_mul_f32_e32 v5, 0xbfb8aa3b, v5
	v_exp_f32_e32 v5, v5
	v_add_u32_e32 v4, 0x47e0, v70
	v_add_f32_e32 v5, 1.0, v5
	v_rcp_f32_e32 v5, v5
	s_nop 0
	v_mul_f32_e32 v5, 0xbf1b459e, v5
	v_mul_f32_e32 v5, 0x3fb8aa3b, v5
	v_exp_f32_e32 v8, v5
	v_mov_b32_e32 v5, v3
	v_lshl_add_u64 v[6:7], v[4:5], 2, s[58:59]
	v_lshl_add_u64 v[4:5], v[4:5], 1, s[56:57]
	global_store_dword v[6:7], v8, off
	v_add_f32_e32 v6, v147, v14
	v_mul_f32_e32 v6, 0xbfb8aa3b, v6
	v_exp_f32_e32 v6, v6
	s_nop 0
	v_add_f32_e32 v6, 1.0, v6
	v_rcp_f32_e32 v6, v6
	s_nop 0
	v_cvt_pk_bf16_f32 v6, v6, s0
	global_store_short v[4:5], v6, off
	v_add_f32_e32 v5, v148, v31
	v_mul_f32_e32 v5, 0xbfb8aa3b, v5
	v_exp_f32_e32 v5, v5
	v_add_u32_e32 v4, 0x4be0, v70
	v_add_f32_e32 v5, 1.0, v5
	v_rcp_f32_e32 v5, v5
	s_nop 0
	v_mul_f32_e32 v5, 0xbf1b459e, v5
	v_mul_f32_e32 v5, 0x3fb8aa3b, v5
	v_exp_f32_e32 v8, v5
	v_mov_b32_e32 v5, v3
	v_lshl_add_u64 v[6:7], v[4:5], 2, s[58:59]
	v_lshl_add_u64 v[4:5], v[4:5], 1, s[56:57]
	global_store_dword v[6:7], v8, off
	v_add_f32_e32 v6, v147, v15
	v_mul_f32_e32 v6, 0xbfb8aa3b, v6
	v_exp_f32_e32 v6, v6
	s_nop 0
	v_add_f32_e32 v6, 1.0, v6
	v_rcp_f32_e32 v6, v6
	s_nop 0
	v_cvt_pk_bf16_f32 v6, v6, s0
	global_store_short v[4:5], v6, off
	v_add_f32_e32 v5, v148, v32
	v_mul_f32_e32 v5, 0xbfb8aa3b, v5
	v_exp_f32_e32 v5, v5
	v_add_u32_e32 v4, 0x5fe0, v70
	v_add_f32_e32 v5, 1.0, v5
	v_rcp_f32_e32 v5, v5
	s_nop 0
	v_mul_f32_e32 v5, 0xbf1b459e, v5
	v_mul_f32_e32 v5, 0x3fb8aa3b, v5
	v_exp_f32_e32 v8, v5
	v_mov_b32_e32 v5, v3
	v_lshl_add_u64 v[6:7], v[4:5], 2, s[58:59]
	v_lshl_add_u64 v[4:5], v[4:5], 1, s[56:57]
	global_store_dword v[6:7], v8, off
	v_add_f32_e32 v6, v147, v16
	v_mul_f32_e32 v6, 0xbfb8aa3b, v6
	v_exp_f32_e32 v6, v6
	s_nop 0
	v_add_f32_e32 v6, 1.0, v6
	v_rcp_f32_e32 v6, v6
	s_nop 0
	v_cvt_pk_bf16_f32 v6, v6, s0
	global_store_short v[4:5], v6, off
	v_add_f32_e32 v5, v148, v33
	v_mul_f32_e32 v5, 0xbfb8aa3b, v5
	v_exp_f32_e32 v5, v5
	v_add_u32_e32 v4, 0x63e0, v70
	v_add_f32_e32 v5, 1.0, v5
	v_rcp_f32_e32 v5, v5
	s_nop 0
	v_mul_f32_e32 v5, 0xbf1b459e, v5
	v_mul_f32_e32 v5, 0x3fb8aa3b, v5
	v_exp_f32_e32 v8, v5
	v_mov_b32_e32 v5, v3
	v_lshl_add_u64 v[6:7], v[4:5], 2, s[58:59]
	v_lshl_add_u64 v[4:5], v[4:5], 1, s[56:57]
	global_store_dword v[6:7], v8, off
	v_add_f32_e32 v6, v147, v17
	v_mul_f32_e32 v6, 0xbfb8aa3b, v6
	v_exp_f32_e32 v6, v6
	s_nop 0
	v_add_f32_e32 v6, 1.0, v6
	v_rcp_f32_e32 v6, v6
	s_nop 0
	v_cvt_pk_bf16_f32 v6, v6, s0
	global_store_short v[4:5], v6, off
	v_add_f32_e32 v5, v148, v34
	v_mul_f32_e32 v5, 0xbfb8aa3b, v5
	v_exp_f32_e32 v5, v5
	v_add_u32_e32 v4, 0x67e0, v70
	v_add_f32_e32 v5, 1.0, v5
	v_rcp_f32_e32 v5, v5
	s_nop 0
	v_mul_f32_e32 v5, 0xbf1b459e, v5
	v_mul_f32_e32 v5, 0x3fb8aa3b, v5
	v_exp_f32_e32 v8, v5
	v_mov_b32_e32 v5, v3
	v_lshl_add_u64 v[6:7], v[4:5], 2, s[58:59]
	v_lshl_add_u64 v[4:5], v[4:5], 1, s[56:57]
	global_store_dword v[6:7], v8, off
	v_add_f32_e32 v6, v147, v18
	v_mul_f32_e32 v6, 0xbfb8aa3b, v6
	v_exp_f32_e32 v6, v6
	s_nop 0
	v_add_f32_e32 v6, 1.0, v6
	v_rcp_f32_e32 v6, v6
	s_nop 0
	v_cvt_pk_bf16_f32 v6, v6, s0
	global_store_short v[4:5], v6, off
	v_add_f32_e32 v5, v148, v35
	v_mul_f32_e32 v5, 0xbfb8aa3b, v5
	v_exp_f32_e32 v5, v5
	v_add_u32_e32 v4, 0x6be0, v70
	s_waitcnt vmcnt(31)
	v_mov_b32_e32 v148, v68
	v_add_f32_e32 v5, 1.0, v5
	v_rcp_f32_e32 v5, v5
	s_nop 0
	v_mul_f32_e32 v5, 0xbf1b459e, v5
	v_mul_f32_e32 v5, 0x3fb8aa3b, v5
	v_exp_f32_e32 v8, v5
	v_mov_b32_e32 v5, v3
	v_lshl_add_u64 v[6:7], v[4:5], 2, s[58:59]
	v_lshl_add_u64 v[4:5], v[4:5], 1, s[56:57]
	global_store_dword v[6:7], v8, off
	v_add_f32_e32 v6, v147, v19
	v_mul_f32_e32 v6, 0xbfb8aa3b, v6
	v_exp_f32_e32 v6, v6
	s_waitcnt vmcnt(31)
	v_mov_b32_e32 v147, v69
	v_add_f32_e32 v6, 1.0, v6
	v_rcp_f32_e32 v6, v6
	s_nop 0
	v_cvt_pk_bf16_f32 v6, v6, s0
	s_add_i32 s0, s0, 32
	s_cmpk_lg_i32 s0, 0xa0
	global_store_short v[4:5], v6, off
	s_cbranch_scc1 .LBB0_285
	s_add_i32 s14, s14, s97
	s_cmpk_gt_i32 s14, 0x1ff
	v_add_u32_e32 v145, s90, v145
	s_barrier
	s_cbranch_scc0 .LBB0_282
